# attention rescale decision: flag cleared on the hot path and set only in the rare rescale block (shorter wave-uniform branch test)
# speedup vs baseline: 1.0031x; 1.0031x over previous
.LBB0_726:
	v_add_u32_e64 v164, s18, v239
	s_add_i32 m0, s38, s30
	s_nop 0
	global_load_lds_dwordx4 v244, s[98:99]
	s_add_i32 m0, s22, s31
	s_nop 0
	global_load_lds_dwordx4 v245, s[98:99]
	s_add_u32 s98, s98, 0x20000
	s_addc_u32 s99, s99, 0
	s_nop 0
	ds_read_b64_tr_b16 v[190:191], v164 offset:24576
	ds_read_b64_tr_b16 v[192:193], v164 offset:25088
	s_waitcnt lgkmcnt(2)
	s_nop 0
	v_mfma_f32_32x32x16_bf16 v[48:63], v[158:161], v[110:113], v[48:63]
	v_add_f32_e32 v114, v80, v81
	v_add_f32_e32 v114, v82, v114
	v_add_f32_e32 v114, v83, v114
	v_add_f32_e32 v114, v84, v114
	v_add_f32_e64 v114, v85, v114
	v_cvt_pk_bf16_f32 v126, v80, v81
	v_cvt_pk_bf16_f32 v127, v82, v83
	ds_read_b64_tr_b16 v[186:187], v164 offset:28672
	ds_read_b64_tr_b16 v[188:189], v164 offset:29184
	v_mfma_f32_32x32x16_bf16 v[32:47], v[146:149], v[110:113], v[32:47]
	v_add_f32_e32 v80, v86, v114
	v_add_f32_e32 v80, v87, v80
	v_add_f32_e32 v80, v88, v80
	v_add_f32_e32 v80, v89, v80
	v_cvt_pk_bf16_f32 v128, v84, v85
	v_cvt_pk_bf16_f32 v129, v86, v87
	ds_read_b64_tr_b16 v[182:183], v164 offset:25600
	ds_read_b64_tr_b16 v[184:185], v164 offset:26112
	v_mfma_f32_32x32x16_bf16 v[48:63], v[154:157], v[106:109], v[48:63]
	v_add_f32_e32 v80, v90, v80
	v_add_f32_e32 v80, v91, v80
	v_add_f32_e32 v80, v92, v80
	v_add_f32_e32 v80, v93, v80
	v_cvt_pk_bf16_f32 v122, v88, v89
	v_cvt_pk_bf16_f32 v123, v90, v91
	ds_read_b64_tr_b16 v[178:179], v164 offset:29696
	ds_read_b64_tr_b16 v[180:181], v164 offset:30208
	v_mfma_f32_32x32x16_bf16 v[32:47], v[142:145], v[106:109], v[32:47]
	v_add_f32_e32 v80, v94, v80
	v_add_f32_e32 v80, v95, v80
	v_add_f32_e32 v80, v64, v80
	v_add_f32_e32 v80, v65, v80
	v_cvt_pk_bf16_f32 v124, v92, v93
	v_cvt_pk_bf16_f32 v125, v94, v95
	ds_read_b64_tr_b16 v[166:167], v164 offset:26624
	ds_read_b64_tr_b16 v[168:169], v164 offset:27136
	v_mfma_f32_32x32x16_bf16 v[48:63], v[150:153], v[102:105], v[48:63]
	v_add_f32_e32 v80, v66, v80
	v_add_f32_e32 v80, v67, v80
	v_add_f32_e32 v80, v68, v80
	v_add_f32_e32 v80, v69, v80
	v_cvt_pk_bf16_f32 v118, v64, v65
	v_cvt_pk_bf16_f32 v119, v66, v67
	ds_read_b64_tr_b16 v[174:175], v164 offset:30720
	ds_read_b64_tr_b16 v[176:177], v164 offset:31232
	v_mfma_f32_32x32x16_bf16 v[32:47], v[138:141], v[102:105], v[32:47]
	v_add_f32_e32 v64, v70, v80
	v_add_f32_e32 v64, v71, v64
	v_add_f32_e32 v64, v72, v64
	v_add_f32_e32 v64, v73, v64
	v_cvt_pk_bf16_f32 v120, v68, v69
	v_cvt_pk_bf16_f32 v121, v70, v71
	ds_read_b64_tr_b16 v[170:171], v164 offset:27648
	ds_read_b64_tr_b16 v[172:173], v164 offset:28160
	v_mfma_f32_32x32x16_bf16 v[48:63], v[134:137], v[98:101], v[48:63]
	v_add_f32_e32 v64, v74, v64
	v_add_f32_e32 v64, v75, v64
	v_add_f32_e32 v64, v76, v64
	v_add_f32_e32 v64, v77, v64
	v_cvt_pk_bf16_f32 v114, v72, v73
	v_cvt_pk_bf16_f32 v115, v74, v75
	ds_read_b64_tr_b16 v[162:163], v164 offset:31744
	ds_read_b64_tr_b16 v[164:165], v164 offset:32256
	v_mfma_f32_32x32x16_bf16 v[32:47], v[130:133], v[98:101], v[32:47]
	v_add_f32_e32 v64, v78, v64
	v_add_f32_e32 v64, v79, v64
	v_add_f32_e64 v224, v240, v64
	v_cvt_pk_bf16_f32 v116, v76, v77
	v_cvt_pk_bf16_f32 v117, v78, v79
	s_waitcnt lgkmcnt(14)
	s_nop 0
	ds_read_b128 v[64:67], v205
	ds_read_b128 v[68:71], v205 offset:32
	ds_read_b128 v[82:85], v205 offset:128
	ds_read_b128 v[86:89], v205 offset:160
	ds_read_b128 v[72:75], v205 offset:64
	ds_read_b128 v[76:79], v205 offset:96
	ds_read_b128 v[90:93], v205 offset:192
	ds_read_b128 v[138:141], v205 offset:224
	v_max_f32_e64 v80, v48, v49
	v_max3_f32 v81, v50, v51, v33
	v_max3_f32 v80, v80, v32, v34
	v_max3_f32 v80, v80, v35, v52
	v_max3_f32 v81, v81, v54, v55
	v_max3_f32 v80, v80, v53, v36
	v_max3_f32 v81, v81, v38, v39
	v_max3_f32 v80, v80, v37, v56
	v_max3_f32 v81, v81, v58, v59
	v_max3_f32 v80, v80, v57, v40
	v_max3_f32 v81, v81, v42, v43
	v_max3_f32 v80, v80, v41, v60
	v_max3_f32 v81, v81, v62, v63
	v_max3_f32 v80, v80, v61, v44
	v_max3_f32 v81, v81, v46, v47
	v_max3_f32 v80, v80, v45, v81
	v_mov_b32_e64 v81, v80
	s_nop 1
	v_permlane32_swap_b32_e32 v80, v81
	v_max_f32_e32 v80, v80, v81
	v_cmp_lt_f32_e32 vcc, s51, v80
	s_mov_b64 s[18:19], 0
	s_cbranch_vccnz .LBB0_734

.LBB0_729:
	s_add_i32 s18, s22, 0x2000
	v_add_u32_e64 v162, s38, v239
	s_cmpk_lg_i32 s22, 0x4000
	s_cselect_b32 s38, s18, 0
	s_add_i32 m0, s22, s30
	s_nop 0
	global_load_lds_dwordx4 v244, s[98:99]
	s_add_i32 m0, s38, s31
	s_nop 0
	global_load_lds_dwordx4 v245, s[98:99]
	s_add_u32 s98, s98, 0x20000
	s_addc_u32 s99, s99, 0
	s_nop 0
	ds_read_b64_tr_b16 v[194:195], v162 offset:24576
	ds_read_b64_tr_b16 v[196:197], v162 offset:25088
	s_waitcnt lgkmcnt(2)
	s_nop 0
	v_mfma_f32_32x32x16_bf16 v[80:95], v[134:137], v[110:113], v[80:95]
	v_add_f32_e32 v114, v48, v49
	v_add_f32_e32 v114, v50, v114
	v_add_f32_e32 v114, v51, v114
	v_add_f32_e32 v114, v52, v114
	v_add_f32_e64 v114, v53, v114
	v_cvt_pk_bf16_f32 v126, v48, v49
	v_cvt_pk_bf16_f32 v127, v50, v51
	ds_read_b64_tr_b16 v[190:191], v162 offset:28672
	ds_read_b64_tr_b16 v[192:193], v162 offset:29184
	v_mfma_f32_32x32x16_bf16 v[64:79], v[130:133], v[110:113], v[64:79]
	v_add_f32_e32 v48, v54, v114
	v_add_f32_e32 v48, v55, v48
	v_add_f32_e32 v48, v56, v48
	v_add_f32_e32 v48, v57, v48
	v_cvt_pk_bf16_f32 v128, v52, v53
	v_cvt_pk_bf16_f32 v129, v54, v55
	ds_read_b64_tr_b16 v[186:187], v162 offset:25600
	ds_read_b64_tr_b16 v[188:189], v162 offset:26112
	v_mfma_f32_32x32x16_bf16 v[80:95], v[146:149], v[106:109], v[80:95]
	v_add_f32_e32 v48, v58, v48
	v_add_f32_e32 v48, v59, v48
	v_add_f32_e32 v48, v60, v48
	v_add_f32_e32 v48, v61, v48
	v_cvt_pk_bf16_f32 v122, v56, v57
	v_cvt_pk_bf16_f32 v123, v58, v59
	ds_read_b64_tr_b16 v[138:139], v162 offset:29696
	ds_read_b64_tr_b16 v[140:141], v162 offset:30208
	v_mfma_f32_32x32x16_bf16 v[64:79], v[142:145], v[106:109], v[64:79]
	v_add_f32_e32 v48, v62, v48
	v_add_f32_e32 v48, v63, v48
	v_add_f32_e32 v48, v32, v48
	v_add_f32_e32 v48, v33, v48
	v_cvt_pk_bf16_f32 v124, v60, v61
	v_cvt_pk_bf16_f32 v125, v62, v63
	ds_read_b64_tr_b16 v[182:183], v162 offset:26624
	ds_read_b64_tr_b16 v[184:185], v162 offset:27136
	v_mfma_f32_32x32x16_bf16 v[80:95], v[158:161], v[102:105], v[80:95]
	v_add_f32_e32 v48, v34, v48
	v_add_f32_e32 v48, v35, v48
	v_add_f32_e32 v48, v36, v48
	v_add_f32_e32 v48, v37, v48
	v_cvt_pk_bf16_f32 v118, v32, v33
	v_cvt_pk_bf16_f32 v119, v34, v35
	ds_read_b64_tr_b16 v[178:179], v162 offset:30720
	ds_read_b64_tr_b16 v[180:181], v162 offset:31232
	v_mfma_f32_32x32x16_bf16 v[64:79], v[154:157], v[102:105], v[64:79]
	v_add_f32_e32 v32, v38, v48
	v_add_f32_e32 v32, v39, v32
	v_add_f32_e32 v32, v40, v32
	v_add_f32_e32 v32, v41, v32
	v_cvt_pk_bf16_f32 v120, v36, v37
	v_cvt_pk_bf16_f32 v121, v38, v39
	ds_read_b64_tr_b16 v[174:175], v162 offset:27648
	ds_read_b64_tr_b16 v[176:177], v162 offset:28160
	v_mfma_f32_32x32x16_bf16 v[80:95], v[166:169], v[98:101], v[80:95]
	v_add_f32_e32 v32, v42, v32
	v_add_f32_e32 v32, v43, v32
	v_add_f32_e32 v32, v44, v32
	v_add_f32_e32 v32, v45, v32
	v_cvt_pk_bf16_f32 v114, v40, v41
	v_cvt_pk_bf16_f32 v115, v42, v43
	ds_read_b64_tr_b16 v[170:171], v162 offset:31744
	ds_read_b64_tr_b16 v[172:173], v162 offset:32256
	v_mfma_f32_32x32x16_bf16 v[64:79], v[150:153], v[98:101], v[64:79]
	v_add_f32_e32 v32, v46, v32
	v_add_f32_e32 v32, v47, v32
	v_add_f32_e64 v240, v224, v32
	v_cvt_pk_bf16_f32 v116, v44, v45
	v_cvt_pk_bf16_f32 v117, v46, v47
	s_waitcnt lgkmcnt(14)
	s_nop 0
	ds_read_b128 v[32:35], v205 offset:256
	ds_read_b128 v[36:39], v205 offset:288
	ds_read_b128 v[50:53], v205 offset:384
	ds_read_b128 v[54:57], v205 offset:416
	ds_read_b128 v[40:43], v205 offset:320
	ds_read_b128 v[44:47], v205 offset:352
	ds_read_b128 v[58:61], v205 offset:448
	ds_read_b128 v[162:165], v205 offset:480
	v_max_f32_e64 v48, v80, v81
	v_max3_f32 v49, v82, v83, v65
	v_max3_f32 v48, v48, v64, v66
	v_max3_f32 v48, v48, v67, v84
	v_max3_f32 v49, v49, v86, v87
	v_max3_f32 v48, v48, v85, v68
	v_max3_f32 v49, v49, v70, v71
	v_max3_f32 v48, v48, v69, v88
	v_max3_f32 v49, v49, v90, v91
	v_max3_f32 v48, v48, v89, v72
	v_max3_f32 v49, v49, v74, v75
	v_max3_f32 v48, v48, v73, v92
	v_max3_f32 v49, v49, v94, v95
	v_max3_f32 v48, v48, v93, v76
	v_max3_f32 v49, v49, v78, v79
	v_max3_f32 v48, v48, v77, v49
	v_mov_b32_e64 v49, v48
	s_nop 1
	v_permlane32_swap_b32_e32 v48, v49
	v_max_f32_e32 v48, v48, v49
	v_cmp_lt_f32_e32 vcc, s51, v48
	s_mov_b64 s[18:19], 0
	s_cbranch_vccnz .LBB0_737

.LBB0_734:
	s_mov_b64 s[18:19], -1
	v_max_f32_e64 v80, v80, v80
	v_max_f32_e64 v81, 0, v80
	v_exp_f32_e64 v80, -v81
	s_and_saveexec_b64 s[20:21], s[2:3]
	s_nop 0
	ds_write_b32 v235, v80 offset:49152
	s_or_b64 exec, exec, s[20:21]
	v_sub_f32_e32 v63, v63, v81
	v_sub_f32_e32 v62, v62, v81
	v_sub_f32_e32 v61, v61, v81
	v_sub_f32_e32 v60, v60, v81
	v_sub_f32_e32 v59, v59, v81
	v_sub_f32_e32 v58, v58, v81
	v_sub_f32_e32 v57, v57, v81
	v_sub_f32_e32 v56, v56, v81
	v_sub_f32_e32 v55, v55, v81
	v_sub_f32_e32 v54, v54, v81
	v_sub_f32_e32 v53, v53, v81
	v_sub_f32_e32 v52, v52, v81
	v_sub_f32_e32 v51, v51, v81
	v_sub_f32_e32 v50, v50, v81
	v_sub_f32_e32 v49, v49, v81
	v_sub_f32_e32 v48, v48, v81
	v_sub_f32_e32 v47, v47, v81
	v_sub_f32_e32 v46, v46, v81
	v_sub_f32_e32 v45, v45, v81
	v_sub_f32_e32 v44, v44, v81
	v_sub_f32_e32 v43, v43, v81
	v_sub_f32_e32 v42, v42, v81
	v_sub_f32_e32 v41, v41, v81
	v_sub_f32_e32 v40, v40, v81
	v_sub_f32_e32 v39, v39, v81
	v_sub_f32_e32 v38, v38, v81
	v_sub_f32_e32 v37, v37, v81
	v_sub_f32_e32 v36, v36, v81
	v_sub_f32_e32 v35, v35, v81
	v_sub_f32_e32 v34, v34, v81
	v_sub_f32_e32 v33, v33, v81
	v_sub_f32_e32 v32, v32, v81
	v_add_f32_e32 v202, v202, v81
	v_mul_f32_e32 v224, v224, v80
	s_branch .LBB0_727
.LBB0_737:
	s_mov_b64 s[18:19], -1
	v_max_f32_e32 v48, v48, v48
	v_max_f32_e64 v49, 0, v48
	v_exp_f32_e64 v48, -v49
	s_and_saveexec_b64 s[20:21], s[2:3]
	s_nop 0
	ds_write_b32 v235, v48 offset:49152
	s_or_b64 exec, exec, s[20:21]
	v_sub_f32_e32 v95, v95, v49
	v_sub_f32_e32 v94, v94, v49
	v_sub_f32_e32 v93, v93, v49
	v_sub_f32_e32 v92, v92, v49
	v_sub_f32_e32 v91, v91, v49
	v_sub_f32_e32 v90, v90, v49
	v_sub_f32_e32 v89, v89, v49
	v_sub_f32_e32 v88, v88, v49
	v_sub_f32_e32 v87, v87, v49
	v_sub_f32_e32 v86, v86, v49
	v_sub_f32_e32 v85, v85, v49
	v_sub_f32_e32 v84, v84, v49
	v_sub_f32_e32 v83, v83, v49
	v_sub_f32_e32 v82, v82, v49
	v_sub_f32_e32 v81, v81, v49
	v_sub_f32_e32 v80, v80, v49
	v_sub_f32_e32 v79, v79, v49
	v_sub_f32_e32 v78, v78, v49
	v_sub_f32_e32 v77, v77, v49
	v_sub_f32_e32 v76, v76, v49
	v_sub_f32_e32 v75, v75, v49
	v_sub_f32_e32 v74, v74, v49
	v_sub_f32_e32 v73, v73, v49
	v_sub_f32_e32 v72, v72, v49
	v_sub_f32_e32 v71, v71, v49
	v_sub_f32_e32 v70, v70, v49
	v_sub_f32_e32 v69, v69, v49
	v_sub_f32_e32 v68, v68, v49
	v_sub_f32_e32 v67, v67, v49
	v_sub_f32_e32 v66, v66, v49
	v_sub_f32_e32 v65, v65, v49
	v_sub_f32_e32 v64, v64, v49
	v_add_f32_e32 v202, v202, v49
	v_mul_f32_e32 v240, v240, v48
	s_branch .LBB0_730
